# baseline (speedup 1.0000x reference)
.LBB1_3:
	s_lshl_b32 s63, s44, 6
	s_lshl_b32 s5, s44, 13
	s_mov_b64 s[44:45], 0x80
	s_and_b32 s62, s10, 3
	s_add_i32 m0, s58, 0x18000
	v_lshl_add_u64 v[8:9], v[8:9], 0, s[44:45]
	s_lshl_b32 s10, s62, 12
	s_waitcnt vmcnt(2)
	s_barrier
	global_load_lds_dwordx4 v[8:9], off
	v_lshl_add_u64 v[6:7], v[6:7], 0, s[44:45]
	s_add_i32 m0, s58, 0x1a000
	s_add_i32 s64, s58, 0x8000
	s_add_i32 s65, s58, 0xa000
	global_load_lds_dwordx4 v[6:7], off
	v_lshl_add_u64 v[2:3], v[2:3], 0, s[44:45]
	s_mov_b32 m0, s64
	s_add_u32 s46, s8, 0x20080
	global_load_lds_dwordx4 v[2:3], off
	v_lshl_add_u64 v[2:3], v[4:5], 0, s[44:45]
	s_mov_b32 m0, s65
	s_addc_u32 s47, s9, 0
	global_load_lds_dwordx4 v[2:3], off
	s_add_i32 m0, s58, 0x1c000
	v_lshl_add_u64 v[2:3], s[46:47], 0, v[164:165]
	global_load_lds_dwordx4 v[2:3], off
	v_lshl_add_u64 v[2:3], s[46:47], 0, v[168:169]
	s_add_i32 m0, s58, 0x1e000
	v_and_b32_e32 v1, 15, v0
	global_load_lds_dwordx4 v[2:3], off
	v_bfe_u32 v3, v0, 4, 2
	v_and_b32_e32 v4, 48, v0
	v_lshlrev_b32_e32 v5, 2, v0
	v_lshlrev_b32_e32 v2, 3, v3
	v_lshl_or_b32 v4, v1, 6, v4
	v_and_b32_e32 v5, 32, v5
	v_lshlrev_b32_e32 v187, 9, v3
	v_lshlrev_b32_e32 v188, 8, v3
	v_lshlrev_b32_e32 v170, 5, v3
	v_lshlrev_b32_e32 v3, 9, v0
	v_bitop3_b32 v6, v4, s5, v5 bitop3:0xde
	v_bitop3_b32 v186, s10, v4, v5 bitop3:0xf6
	v_and_b32_e32 v3, 0x30000, v3
	v_lshlrev_b32_e32 v4, 12, v12
	v_or3_b32 v3, v10, v3, v4
	s_or_b32 s66, s62, 0x7fe0
	s_or_b32 s67, s62, 0x7fd8
	v_add_u32_e32 v176, v3, v11
	v_lshlrev_b32_e32 v3, 5, v13
	s_waitcnt vmcnt(6)
	s_cmpk_lt_u32 s1, 0x100
	v_and_b32_e32 v3, 0x70000, v3
	s_cselect_b64 s[46:47], -1, 0
	v_lshl_or_b32 v190, v1, 5, v2
	v_or3_b32 v3, v10, v3, v4
	s_add_i32 s68, 0, 0x10000
	s_add_i32 s69, 0, 0x14000
	v_lshlrev_b32_e32 v194, 2, v2
	v_mbcnt_lo_u32_b32 v2, -1, 0
	s_sext_i32_i8 s77, s0
	v_lshlrev_b32_e32 v189, 3, v1
	v_lshl_add_u64 v[172:173], s[26:27], 0, v[170:171]
	v_lshl_add_u64 v[174:175], s[36:37], 0, v[170:171]
	v_mov_b32_e32 v177, v171
	v_add_u32_e32 v178, v3, v11
	v_mov_b32_e32 v179, v171
	v_mov_b64_e32 v[180:181], 0xc0
	v_mov_b64_e32 v[182:183], 0xbf
	v_add_u32_e32 v191, s68, v186
	v_add_u32_e32 v192, s69, v186
	v_add_u32_e32 v193, 0, v6
	v_mov_b32_e32 v195, 0x358637bd
	s_mov_b32 s70, 0xf800000
	v_mov_b32_e32 v196, 0x260
	s_movk_i32 s71, 0x1000
	s_movk_i32 s72, 0x800
	s_movk_i32 s73, 0x7df
	s_movk_i32 s74, 0x7ef
	s_movk_i32 s75, 0x7ff
	v_mov_b32_e32 v197, 0x3e38aa3b
	v_mbcnt_hi_u32_b32 v198, -1, v2
	s_mov_b32 s76, 0
	s_barrier
	s_and_b64 vcc, exec, s[46:47]
	s_cbranch_vccnz .Lqkv_noprio
	s_setprio 1
.Lqkv_noprio:
	s_branch .LBB1_6

.Lqkv_nopoll:
	ds_read_b128 v[130:133], v191
	ds_read_b128 v[134:137], v191 offset:1024
	ds_read_b128 v[138:141], v191 offset:2048
	ds_read_b128 v[142:145], v191 offset:3072
	ds_read_b128 v[146:149], v192
	ds_read_b128 v[150:153], v192 offset:1024
	ds_read_b128 v[154:157], v192 offset:2048
	ds_read_b128 v[158:161], v192 offset:3072
	s_add_u32 s8, s6, 0xfff80080
	s_addc_u32 s9, s7, -1
	s_cmp_eq_u32 s56, 28
	s_cselect_b32 s53, s5, s9
	s_cselect_b32 s52, s10, s8
	s_cselect_b32 s9, s27, s55
	s_cselect_b32 s8, s37, s54
	v_lshl_add_u64 v[184:185], s[6:7], 0, v[176:177]
	s_add_i32 m0, s58, 0xc000
	ds_read_b128 v[200:203], v193
	ds_read_b128 v[204:207], v193 offset:1024
	ds_read_b128 v[208:211], v193 offset:2048
	ds_read_b128 v[212:215], v193 offset:3072
	ds_read_b128 v[216:219], v193 offset:4096
	ds_read_b128 v[220:223], v193 offset:5120
	ds_read_b128 v[224:227], v193 offset:6144
	ds_read_b128 v[228:231], v193 offset:7168
	global_load_lds_dwordx4 v[184:185], off
	v_lshl_add_u64 v[184:185], s[6:7], 0, v[178:179]
	s_add_i32 m0, s58, 0xe000
	s_nop 0
	global_load_lds_dwordx4 v[184:185], off
	s_waitcnt vmcnt(8)
	s_waitcnt lgkmcnt(0)
	s_barrier
	s_nop 0
	s_waitcnt lgkmcnt(0)
	v_mfma_f32_16x16x32_f16 v[126:129], v[130:133], v[200:203], v[126:129]
	v_mfma_f32_16x16x32_f16 v[122:125], v[138:141], v[200:203], v[122:125]
	v_mfma_f32_16x16x32_f16 v[118:121], v[130:133], v[208:211], v[118:121]
	v_mfma_f32_16x16x32_f16 v[114:117], v[138:141], v[208:211], v[114:117]
	v_mfma_f32_16x16x32_f16 v[102:105], v[130:133], v[216:219], v[102:105]
	v_mfma_f32_16x16x32_f16 v[98:101], v[138:141], v[216:219], v[98:101]
	v_mfma_f32_16x16x32_f16 v[86:89], v[130:133], v[224:227], v[86:89]
	v_mfma_f32_16x16x32_f16 v[82:85], v[138:141], v[224:227], v[82:85]
	v_mfma_f32_16x16x32_f16 v[126:129], v[134:137], v[204:207], v[126:129]
	v_mfma_f32_16x16x32_f16 v[122:125], v[142:145], v[204:207], v[122:125]
	v_mfma_f32_16x16x32_f16 v[118:121], v[134:137], v[212:215], v[118:121]
	v_mfma_f32_16x16x32_f16 v[114:117], v[142:145], v[212:215], v[114:117]
	v_mfma_f32_16x16x32_f16 v[102:105], v[134:137], v[220:223], v[102:105]
	v_mfma_f32_16x16x32_f16 v[98:101], v[142:145], v[220:223], v[98:101]
	v_mfma_f32_16x16x32_f16 v[86:89], v[134:137], v[228:231], v[86:89]
	v_mfma_f32_16x16x32_f16 v[82:85], v[142:145], v[228:231], v[82:85]
	s_nop 0
	s_nop 0
	v_mfma_f32_16x16x32_f16 v[110:113], v[146:149], v[200:203], v[110:113]
	v_mfma_f32_16x16x32_f16 v[106:109], v[154:157], v[200:203], v[106:109]
	v_mfma_f32_16x16x32_f16 v[94:97], v[146:149], v[208:211], v[94:97]
	v_mfma_f32_16x16x32_f16 v[90:93], v[154:157], v[208:211], v[90:93]
	v_mfma_f32_16x16x32_f16 v[78:81], v[146:149], v[216:219], v[78:81]
	v_mfma_f32_16x16x32_f16 v[74:77], v[154:157], v[216:219], v[74:77]
	v_mfma_f32_16x16x32_f16 v[70:73], v[146:149], v[224:227], v[70:73]
	v_mfma_f32_16x16x32_f16 v[66:69], v[154:157], v[224:227], v[66:69]
	v_mfma_f32_16x16x32_f16 v[110:113], v[150:153], v[204:207], v[110:113]
	v_mfma_f32_16x16x32_f16 v[106:109], v[158:161], v[204:207], v[106:109]
	v_mfma_f32_16x16x32_f16 v[94:97], v[150:153], v[212:215], v[94:97]
	v_mfma_f32_16x16x32_f16 v[90:93], v[158:161], v[212:215], v[90:93]
	v_mfma_f32_16x16x32_f16 v[78:81], v[150:153], v[220:223], v[78:81]
	v_mfma_f32_16x16x32_f16 v[74:77], v[158:161], v[220:223], v[74:77]
	v_mfma_f32_16x16x32_f16 v[70:73], v[150:153], v[228:231], v[70:73]
	v_mfma_f32_16x16x32_f16 v[66:69], v[158:161], v[228:231], v[66:69]
	s_nop 0
	s_barrier
	s_add_i32 s57, s68, s3
	v_lshl_add_u64 v[184:185], s[8:9], 0, v[164:165]
	s_mov_b32 m0, s57
	ds_read_b128 v[200:203], v193 offset:16384
	ds_read_b128 v[204:207], v193 offset:17408
	ds_read_b128 v[208:211], v193 offset:18432
	ds_read_b128 v[212:215], v193 offset:19456
	ds_read_b128 v[216:219], v193 offset:20480
	ds_read_b128 v[220:223], v193 offset:21504
	ds_read_b128 v[224:227], v193 offset:22528
	ds_read_b128 v[228:231], v193 offset:23552
	global_load_lds_dwordx4 v[184:185], off
	s_add_i32 m0, s57, 0x2000
	s_add_u32 s78, s8, 0x20000
	v_lshl_add_u64 v[232:233], s[8:9], 0, v[168:169]
	s_addc_u32 s79, s9, 0
	s_add_i32 s57, s69, s3
	global_load_lds_dwordx4 v[232:233], off
	v_lshl_add_u64 v[234:235], s[78:79], 0, v[164:165]
	s_mov_b32 m0, s57
	v_lshl_add_u64 v[236:237], s[52:53], 0, v[166:167]
	global_load_lds_dwordx4 v[234:235], off
	v_lshl_add_u64 v[234:235], s[78:79], 0, v[168:169]
	s_add_i32 m0, s57, 0x2000
	s_nop 0
	global_load_lds_dwordx4 v[234:235], off
	v_lshl_add_u64 v[234:235], s[52:53], 0, v[162:163]
	s_mov_b32 m0, s58
	s_nop 0
	global_load_lds_dwordx4 v[234:235], off
	s_mov_b32 m0, s59
	s_nop 0
	global_load_lds_dwordx4 v[236:237], off
	s_waitcnt vmcnt(8)
	s_waitcnt lgkmcnt(0)
	s_barrier
	s_nop 0
	s_waitcnt lgkmcnt(0)
	v_mfma_f32_16x16x32_f16 v[62:65], v[130:133], v[200:203], v[62:65]
	v_mfma_f32_16x16x32_f16 v[58:61], v[138:141], v[200:203], v[58:61]
	v_mfma_f32_16x16x32_f16 v[54:57], v[130:133], v[208:211], v[54:57]
	v_mfma_f32_16x16x32_f16 v[50:53], v[138:141], v[208:211], v[50:53]
	v_mfma_f32_16x16x32_f16 v[38:41], v[130:133], v[216:219], v[38:41]
	v_mfma_f32_16x16x32_f16 v[34:37], v[138:141], v[216:219], v[34:37]
	v_mfma_f32_16x16x32_f16 v[22:25], v[130:133], v[224:227], v[22:25]
	v_mfma_f32_16x16x32_f16 v[18:21], v[138:141], v[224:227], v[18:21]
	v_mfma_f32_16x16x32_f16 v[62:65], v[134:137], v[204:207], v[62:65]
	v_mfma_f32_16x16x32_f16 v[58:61], v[142:145], v[204:207], v[58:61]
	v_mfma_f32_16x16x32_f16 v[54:57], v[134:137], v[212:215], v[54:57]
	v_mfma_f32_16x16x32_f16 v[50:53], v[142:145], v[212:215], v[50:53]
	v_mfma_f32_16x16x32_f16 v[38:41], v[134:137], v[220:223], v[38:41]
	v_mfma_f32_16x16x32_f16 v[34:37], v[142:145], v[220:223], v[34:37]
	v_mfma_f32_16x16x32_f16 v[22:25], v[134:137], v[228:231], v[22:25]
	v_mfma_f32_16x16x32_f16 v[18:21], v[142:145], v[228:231], v[18:21]
	s_nop 0
	s_nop 0
	v_mfma_f32_16x16x32_f16 v[46:49], v[146:149], v[200:203], v[46:49]
	v_mfma_f32_16x16x32_f16 v[42:45], v[154:157], v[200:203], v[42:45]
	v_mfma_f32_16x16x32_f16 v[30:33], v[146:149], v[208:211], v[30:33]
	v_mfma_f32_16x16x32_f16 v[26:29], v[154:157], v[208:211], v[26:29]
	v_mfma_f32_16x16x32_f16 v[14:17], v[146:149], v[216:219], v[14:17]
	v_mfma_f32_16x16x32_f16 v[10:13], v[154:157], v[216:219], v[10:13]
	v_mfma_f32_16x16x32_f16 v[6:9], v[146:149], v[224:227], v[6:9]
	v_mfma_f32_16x16x32_f16 v[2:5], v[154:157], v[224:227], v[2:5]
	v_mfma_f32_16x16x32_f16 v[46:49], v[150:153], v[204:207], v[46:49]
	v_mfma_f32_16x16x32_f16 v[42:45], v[158:161], v[204:207], v[42:45]
	v_mfma_f32_16x16x32_f16 v[30:33], v[150:153], v[212:215], v[30:33]
	v_mfma_f32_16x16x32_f16 v[26:29], v[158:161], v[212:215], v[26:29]
	v_mfma_f32_16x16x32_f16 v[14:17], v[150:153], v[220:223], v[14:17]
	v_mfma_f32_16x16x32_f16 v[10:13], v[158:161], v[220:223], v[10:13]
	v_mfma_f32_16x16x32_f16 v[6:9], v[150:153], v[228:231], v[6:9]
	v_mfma_f32_16x16x32_f16 v[2:5], v[158:161], v[228:231], v[2:5]
	s_nop 0
	s_barrier
	s_add_i32 s57, 0, 0x18000
	s_add_i32 s78, 0, 0x1c000
	v_add_u32_e32 v142, s57, v186
	v_add_u32_e32 v158, s78, v186
	ds_read_b128 v[130:133], v142
	ds_read_b128 v[134:137], v142 offset:1024
	ds_read_b128 v[138:141], v142 offset:2048
	ds_read_b128 v[142:145], v142 offset:3072
	ds_read_b128 v[146:149], v158
	ds_read_b128 v[150:153], v158 offset:1024
	ds_read_b128 v[154:157], v158 offset:2048
	ds_read_b128 v[158:161], v158 offset:3072
	s_add_u32 s52, s52, 0x80000
	s_addc_u32 s53, s53, 0
	s_mov_b32 m0, s60
	v_lshl_add_u64 v[238:239], s[52:53], 0, v[162:163]
	ds_read_b128 v[200:203], v193 offset:32768
	ds_read_b128 v[204:207], v193 offset:33792
	ds_read_b128 v[208:211], v193 offset:34816
	ds_read_b128 v[212:215], v193 offset:35840
	ds_read_b128 v[216:219], v193 offset:36864
	ds_read_b128 v[220:223], v193 offset:37888
	ds_read_b128 v[224:227], v193 offset:38912
	ds_read_b128 v[228:231], v193 offset:39936
	global_load_lds_dwordx4 v[238:239], off
	v_lshl_add_u64 v[238:239], s[52:53], 0, v[166:167]
	s_mov_b32 m0, s61
	s_nop 0
	global_load_lds_dwordx4 v[238:239], off
	s_waitcnt vmcnt(8)
	s_waitcnt lgkmcnt(0)
	s_barrier
	s_nop 0
	s_waitcnt lgkmcnt(0)
	v_mfma_f32_16x16x32_f16 v[126:129], v[130:133], v[200:203], v[126:129]
	v_mfma_f32_16x16x32_f16 v[122:125], v[138:141], v[200:203], v[122:125]
	v_mfma_f32_16x16x32_f16 v[118:121], v[130:133], v[208:211], v[118:121]
	v_mfma_f32_16x16x32_f16 v[114:117], v[138:141], v[208:211], v[114:117]
	v_mfma_f32_16x16x32_f16 v[102:105], v[130:133], v[216:219], v[102:105]
	v_mfma_f32_16x16x32_f16 v[98:101], v[138:141], v[216:219], v[98:101]
	v_mfma_f32_16x16x32_f16 v[86:89], v[130:133], v[224:227], v[86:89]
	v_mfma_f32_16x16x32_f16 v[82:85], v[138:141], v[224:227], v[82:85]
	v_mfma_f32_16x16x32_f16 v[126:129], v[134:137], v[204:207], v[126:129]
	v_mfma_f32_16x16x32_f16 v[122:125], v[142:145], v[204:207], v[122:125]
	v_mfma_f32_16x16x32_f16 v[118:121], v[134:137], v[212:215], v[118:121]
	v_mfma_f32_16x16x32_f16 v[114:117], v[142:145], v[212:215], v[114:117]
	v_mfma_f32_16x16x32_f16 v[102:105], v[134:137], v[220:223], v[102:105]
	v_mfma_f32_16x16x32_f16 v[98:101], v[142:145], v[220:223], v[98:101]
	v_mfma_f32_16x16x32_f16 v[86:89], v[134:137], v[228:231], v[86:89]
	v_mfma_f32_16x16x32_f16 v[82:85], v[142:145], v[228:231], v[82:85]
	s_nop 0
	s_nop 0
	v_mfma_f32_16x16x32_f16 v[110:113], v[146:149], v[200:203], v[110:113]
	v_mfma_f32_16x16x32_f16 v[106:109], v[154:157], v[200:203], v[106:109]
	v_mfma_f32_16x16x32_f16 v[94:97], v[146:149], v[208:211], v[94:97]
	v_mfma_f32_16x16x32_f16 v[90:93], v[154:157], v[208:211], v[90:93]
	v_mfma_f32_16x16x32_f16 v[78:81], v[146:149], v[216:219], v[78:81]
	v_mfma_f32_16x16x32_f16 v[74:77], v[154:157], v[216:219], v[74:77]
	v_mfma_f32_16x16x32_f16 v[70:73], v[146:149], v[224:227], v[70:73]
	v_mfma_f32_16x16x32_f16 v[66:69], v[154:157], v[224:227], v[66:69]
	v_mfma_f32_16x16x32_f16 v[110:113], v[150:153], v[204:207], v[110:113]
	v_mfma_f32_16x16x32_f16 v[106:109], v[158:161], v[204:207], v[106:109]
	v_mfma_f32_16x16x32_f16 v[94:97], v[150:153], v[212:215], v[94:97]
	v_mfma_f32_16x16x32_f16 v[90:93], v[158:161], v[212:215], v[90:93]
	v_mfma_f32_16x16x32_f16 v[78:81], v[150:153], v[220:223], v[78:81]
	v_mfma_f32_16x16x32_f16 v[74:77], v[158:161], v[220:223], v[74:77]
	v_mfma_f32_16x16x32_f16 v[70:73], v[150:153], v[228:231], v[70:73]
	v_mfma_f32_16x16x32_f16 v[66:69], v[158:161], v[228:231], v[66:69]
	s_nop 0
	s_barrier
	s_add_i32 s52, s57, s3
	v_lshl_add_u64 v[184:185], v[184:185], 0, s[44:45]
	s_mov_b32 m0, s52
	ds_read_b128 v[200:203], v193 offset:49152
	ds_read_b128 v[204:207], v193 offset:50176
	ds_read_b128 v[208:211], v193 offset:51200
	ds_read_b128 v[212:215], v193 offset:52224
	ds_read_b128 v[216:219], v193 offset:53248
	ds_read_b128 v[220:223], v193 offset:54272
	ds_read_b128 v[224:227], v193 offset:55296
	ds_read_b128 v[228:231], v193 offset:56320
	global_load_lds_dwordx4 v[184:185], off
	s_add_i32 m0, s52, 0x2000
	s_add_u32 s8, s8, 0x20080
	v_lshl_add_u64 v[184:185], v[232:233], 0, s[44:45]
	s_addc_u32 s9, s9, 0
	s_add_i32 s52, s78, s3
	global_load_lds_dwordx4 v[184:185], off
	v_lshl_add_u64 v[184:185], s[8:9], 0, v[164:165]
	s_mov_b32 m0, s52
	s_nop 0
	global_load_lds_dwordx4 v[184:185], off
	v_lshl_add_u64 v[184:185], s[8:9], 0, v[168:169]
	s_add_i32 m0, s52, 0x2000
	s_nop 0
	global_load_lds_dwordx4 v[184:185], off
	v_lshl_add_u64 v[184:185], v[234:235], 0, s[44:45]
	s_mov_b32 m0, s64
	s_nop 0
	global_load_lds_dwordx4 v[184:185], off
	v_lshl_add_u64 v[184:185], v[236:237], 0, s[44:45]
	s_mov_b32 m0, s65
	s_nop 0
	global_load_lds_dwordx4 v[184:185], off
	s_waitcnt vmcnt(8)
	s_waitcnt lgkmcnt(0)
	s_barrier
	s_nop 0
	s_waitcnt lgkmcnt(0)
	v_mfma_f32_16x16x32_f16 v[62:65], v[130:133], v[200:203], v[62:65]
	v_mfma_f32_16x16x32_f16 v[58:61], v[138:141], v[200:203], v[58:61]
	v_mfma_f32_16x16x32_f16 v[54:57], v[130:133], v[208:211], v[54:57]
	v_mfma_f32_16x16x32_f16 v[50:53], v[138:141], v[208:211], v[50:53]
	v_mfma_f32_16x16x32_f16 v[38:41], v[130:133], v[216:219], v[38:41]
	v_mfma_f32_16x16x32_f16 v[34:37], v[138:141], v[216:219], v[34:37]
	v_mfma_f32_16x16x32_f16 v[22:25], v[130:133], v[224:227], v[22:25]
	v_mfma_f32_16x16x32_f16 v[18:21], v[138:141], v[224:227], v[18:21]
	v_mfma_f32_16x16x32_f16 v[62:65], v[134:137], v[204:207], v[62:65]
	v_mfma_f32_16x16x32_f16 v[58:61], v[142:145], v[204:207], v[58:61]
	v_mfma_f32_16x16x32_f16 v[54:57], v[134:137], v[212:215], v[54:57]
	v_mfma_f32_16x16x32_f16 v[50:53], v[142:145], v[212:215], v[50:53]
	v_mfma_f32_16x16x32_f16 v[38:41], v[134:137], v[220:223], v[38:41]
	v_mfma_f32_16x16x32_f16 v[34:37], v[142:145], v[220:223], v[34:37]
	v_mfma_f32_16x16x32_f16 v[22:25], v[134:137], v[228:231], v[22:25]
	v_mfma_f32_16x16x32_f16 v[18:21], v[142:145], v[228:231], v[18:21]
	s_nop 0
	s_nop 0
	v_mfma_f32_16x16x32_f16 v[46:49], v[146:149], v[200:203], v[46:49]
	v_mfma_f32_16x16x32_f16 v[42:45], v[154:157], v[200:203], v[42:45]
	v_mfma_f32_16x16x32_f16 v[30:33], v[146:149], v[208:211], v[30:33]
	v_mfma_f32_16x16x32_f16 v[26:29], v[154:157], v[208:211], v[26:29]
	v_mfma_f32_16x16x32_f16 v[14:17], v[146:149], v[216:219], v[14:17]
	v_mfma_f32_16x16x32_f16 v[10:13], v[154:157], v[216:219], v[10:13]
	v_mfma_f32_16x16x32_f16 v[6:9], v[146:149], v[224:227], v[6:9]
	v_mfma_f32_16x16x32_f16 v[2:5], v[154:157], v[224:227], v[2:5]
	v_mfma_f32_16x16x32_f16 v[46:49], v[150:153], v[204:207], v[46:49]
	v_mfma_f32_16x16x32_f16 v[42:45], v[158:161], v[204:207], v[42:45]
	v_mfma_f32_16x16x32_f16 v[30:33], v[150:153], v[212:215], v[30:33]
	v_mfma_f32_16x16x32_f16 v[26:29], v[158:161], v[212:215], v[26:29]
	v_mfma_f32_16x16x32_f16 v[14:17], v[150:153], v[220:223], v[14:17]
	v_mfma_f32_16x16x32_f16 v[10:13], v[158:161], v[220:223], v[10:13]
	v_mfma_f32_16x16x32_f16 v[6:9], v[150:153], v[228:231], v[6:9]
	v_mfma_f32_16x16x32_f16 v[2:5], v[158:161], v[228:231], v[2:5]
	s_nop 0
	s_barrier
	s_add_i32 s56, s56, 2
	s_add_u32 s6, s6, 0x100
	s_addc_u32 s7, s7, 0
	s_add_u32 s54, s54, 0x100
	s_addc_u32 s55, s55, 0
	s_cmp_gt_u32 s56, 29
	s_cbranch_scc0 .LBB1_9
	s_and_b64 vcc, exec, s[46:47]
	s_cbranch_vccz .LBB1_12
	s_barrier
